# MoE2 and LN2 reuse the expert tables MoE1 left in LDS; LN2 loads te/tpos for both tokens and next group up front so row loads issue back to back
# speedup vs baseline: 1.0189x; 1.0001x over previous
.LBB0_3431:
	v_readlane_b32 s0, v253, 54
	s_nop 1
	v_mov_b32_e32 v1, s0
	s_waitcnt vmcnt(0)
	ds_read_b64 v[2:3], v1
	v_readlane_b32 s0, v253, 38
	s_waitcnt lgkmcnt(0)
	v_readfirstlane_b32 s6, v3
	v_mov_b32_e32 v1, s0
	v_readfirstlane_b32 s7, v2
	ds_read_b64 v[2:3], v1
	v_mov_b32_e32 v1, v0
	s_waitcnt lgkmcnt(0)
	v_cmp_gt_i32_e32 vcc, 64, v1
	v_readfirstlane_b32 s8, v3
	v_readfirstlane_b32 s9, v2


	v_readlane_b32 s0, v253, 5
	v_readlane_b32 s10, v253, 0
	v_readlane_b32 s1, v253, 6
	v_readlane_b32 s12, v253, 3
	s_waitcnt lgkmcnt(0)

	s_load_dword s11, s[0:1], 0x0
	s_cmpk_gt_i32 s10, 0x1ff
	v_readlane_b32 s13, v253, 4
	s_waitcnt lgkmcnt(0)
	s_cbranch_scc1 .LBB0_3493
	s_add_u32 s0, s9, 0x204e0000
	s_addc_u32 s1, s8, 0
	s_add_u32 s12, s9, 0x21ce0000
	v_readlane_b32 s2, v254, 1
	s_addc_u32 s13, s8, 0
	s_lshl_b32 s64, s2, 25
	s_lshl_b64 s[2:3], s[64:65], 2
	s_add_u32 s14, s7, s2
	s_addc_u32 s15, s6, s3
	s_branch .LBB0_3441

.LBB0_3533:
	v_readlane_b32 s0, v253, 49
	v_mov_b32_e32 v70, v0
	s_nop 0
	v_mov_b32_e32 v1, s0
	s_waitcnt vmcnt(0)
	ds_read2_b64 v[2:5], v1 offset1:1
	v_readlane_b32 s0, v253, 55
	s_waitcnt lgkmcnt(0)
	v_readfirstlane_b32 s2, v2
	v_mov_b32_e32 v1, s0
	v_readlane_b32 s0, v253, 56
	ds_read_b64 v[14:15], v1
	v_readfirstlane_b32 s3, v3
	v_mov_b32_e32 v1, s0
	v_readlane_b32 s0, v254, 1
	s_lshl_b32 s0, s0, 12
	s_or_b32 s64, s0, 0x800
	s_lshl_b64 s[0:1], s[64:65], 2
	s_add_u32 s2, s2, s0
	v_readfirstlane_b32 s4, v5
	v_readfirstlane_b32 s5, v4
	ds_read_b128 v[2:5], v1
	s_addc_u32 s3, s3, s1
	s_add_u32 s0, s5, s0
	v_ashrrev_i32_e32 v71, 31, v70
	v_lshlrev_b64 v[10:11], 4, v[70:71]
	s_addc_u32 s1, s4, s1
	v_lshl_add_u64 v[6:7], s[2:3], 0, v[10:11]
	global_load_dwordx4 v[6:9], v[6:7], off
	v_lshl_add_u64 v[10:11], s[0:1], 0, v[10:11]
	global_load_dwordx4 v[10:13], v[10:11], off
	v_lshl_add_u32 v16, v70, 4, 0
	v_readfirstlane_b32 s12, v70
	v_and_b32_e32 v1, 63, v70
	v_add_u32_e32 v17, 0x18000, v16
	s_waitcnt lgkmcnt(1)
	v_readfirstlane_b32 s3, v15
	v_readfirstlane_b32 s2, v14
	s_waitcnt lgkmcnt(0)
	v_readfirstlane_b32 s11, v3
	v_readfirstlane_b32 s10, v2
	v_readfirstlane_b32 s5, v5
	v_readfirstlane_b32 s4, v4
	v_readlane_b32 s8, v253, 5
	v_readlane_b32 s9, v253, 6
	v_readlane_b32 s14, v253, 0
	s_ashr_i32 s13, s12, 6
	s_lshl_b32 s13, s13, 4
	s_nop 1
	s_load_dword s15, s[8:9], 0x0
	s_lshl_b32 s16, s14, 7
	s_add_i32 s13, s13, s16
	s_add_u32 s16, s4, 0x202b0000
	s_addc_u32 s17, s5, 0
	s_add_u32 s16, s16, s13
	s_addc_u32 s17, s17, 0
	global_load_dwordx4 v[32:35], v87, s[16:17]
	s_add_u32 s16, s4, 0x202c0000
	s_addc_u32 s17, s5, 0
	s_add_u32 s16, s16, s13
	s_addc_u32 s17, s17, 0
	global_load_dwordx4 v[224:227], v87, s[16:17]
	s_mov_b32 s32, 0
	s_waitcnt lgkmcnt(0)
	s_add_i32 s14, s14, s15
	s_cmpk_lt_i32 s14, 0x200
	s_cbranch_scc0 .Lln2_nopre
	s_lshl_b32 s15, s15, 7
	s_add_i32 s13, s13, s15
	s_add_u32 s16, s4, 0x202b0000
	s_addc_u32 s17, s5, 0
	s_add_u32 s16, s16, s13
	s_addc_u32 s17, s17, 0
	global_load_dwordx4 v[242:245], v87, s[16:17]
	s_add_u32 s16, s4, 0x202c0000
	s_addc_u32 s17, s5, 0
	s_add_u32 s16, s16, s13
	s_addc_u32 s17, s17, 0
	global_load_dwordx4 v[246:249], v87, s[16:17]
	s_mov_b32 s32, 1
.Lln2_nopre:
	v_cmp_gt_i32_e32 vcc, 64, v70
	v_add_u32_e32 v16, 0x1a000, v16
	s_waitcnt vmcnt(0)
	ds_write_b128 v17, v[6:9]
	s_waitcnt vmcnt(0)
	ds_write_b128 v16, v[10:13]


	v_readlane_b32 s0, v253, 5
	v_readlane_b32 s1, v253, 6
	s_waitcnt lgkmcnt(0)
	s_barrier
	s_load_dword s18, s[0:1], 0x0
	v_readlane_b32 s20, v253, 0
	s_waitcnt lgkmcnt(0)
	s_cmpk_gt_i32 s20, 0x1ff
	s_cbranch_scc0 .LBB0_3539
	s_getpc_b64 s[98:99]

.LBB0_3539:
	s_add_u32 s6, s4, 0x6030000
	s_addc_u32 s7, s5, 0
	s_add_u32 s21, s4, 0xa030000
	s_addc_u32 s22, s5, 0
	s_add_u32 s23, s4, 0x202b0000
	s_addc_u32 s24, s5, 0
	s_add_u32 s25, s4, 0x202c0000
	s_addc_u32 s26, s5, 0
	s_add_u32 s0, s4, 0x21ce0000
	s_addc_u32 s1, s5, 0
	v_readlane_b32 s8, v254, 1
	s_cmp_eq_u32 s8, 3
	s_cselect_b64 s[8:9], -1, 0
	s_cmp_lg_u64 s[10:11], 0
	s_cselect_b64 s[14:15], -1, 0
	s_ashr_i32 s19, s12, 6
	s_lshl_b32 s27, s20, 4
	s_lshl_b32 s28, s19, 1
	s_add_i32 s12, s27, s28
	s_and_b64 s[8:9], s[8:9], s[14:15]
	s_lshl_b32 s14, s12, 1
	s_ashr_i32 s15, s14, 31
	s_lshl_b64 s[14:15], s[14:15], 2
	s_add_u32 s16, s23, s14
	s_addc_u32 s17, s24, s15

	s_add_i32 s29, 0, 0x230a0
	s_add_u32 s14, s25, s14
	s_addc_u32 s15, s26, s15
	s_ashr_i32 s13, s12, 31
	v_lshlrev_b32_e32 v72, 2, v1
	v_or_b32_e32 v76, 0x400, v72
	v_or_b32_e32 v78, 0x500, v72
	v_or_b32_e32 v80, 0x600, v72
	v_or_b32_e32 v82, 0x700, v72
	v_lshlrev_b32_e32 v74, 4, v1
	v_lshlrev_b32_e32 v66, 3, v1
	v_lshlrev_b32_e32 v68, 2, v76
	v_lshlrev_b32_e32 v126, 2, v78
	v_lshlrev_b32_e32 v128, 2, v80
	v_lshlrev_b32_e32 v130, 2, v82
	v_xor_b32_e32 v71, 16, v215
	v_xor_b32_e32 v73, 8, v215
	v_xor_b32_e32 v77, 4, v215
	v_mov_b32_e32 v67, v87
	v_xor_b32_e32 v79, 2, v215
	v_xor_b32_e32 v83, 1, v215
	v_or_b32_e32 v86, 0x400, v74
	v_lshl_add_u64 v[134:135], s[0:1], 0, v[66:67]
	v_mov_b32_e32 v75, v87
	v_mov_b32_e32 v69, v87
	v_mov_b32_e32 v127, v87
	v_mov_b32_e32 v129, v87
	v_mov_b32_e32 v131, v87
	v_lshl_add_u64 v[122:123], s[10:11], 0, v[74:75]
	v_lshl_add_u64 v[124:125], s[10:11], 0, v[68:69]
	s_waitcnt vmcnt(0)
	v_lshlrev_b32_e32 v2, 2, v32
	v_add_u32_e32 v2, s29, v2
	ds_read_b32 v5, v2
	v_lshlrev_b32_e32 v2, 2, v33
	v_add_u32_e32 v2, s29, v2
	ds_read_b32 v4, v2
	v_mov_b32_e32 v2, v224
	v_mov_b32_e32 v3, v225
	s_lshl_b64 s[14:15], s[12:13], 13
	s_add_u32 s14, s21, s14
	s_addc_u32 s15, s22, s15
	s_or_b32 s12, s12, 1
	v_lshlrev_b32_e32 v1, 2, v34
	v_add_u32_e32 v1, s29, v1
	s_waitcnt vmcnt(0) lgkmcnt(0)
	v_add_u32_e32 v4, v3, v4
	v_add_u32_e32 v2, v2, v5
	v_ashrrev_i32_e32 v3, 31, v2
	v_ashrrev_i32_e32 v5, 31, v4
	v_lshlrev_b64 v[4:5], 12, v[4:5]
	v_lshlrev_b64 v[2:3], 12, v[2:3]
	v_lshl_add_u64 v[6:7], s[0:1], 0, v[2:3]
	v_lshl_add_u64 v[8:9], s[0:1], 0, v[4:5]
	v_readfirstlane_b32 s16, v6
	v_readfirstlane_b32 s17, v7
	v_readfirstlane_b32 s30, v8
	v_readfirstlane_b32 s31, v9
	global_load_dwordx4 v[2:5], v74, s[14:15] nt
	s_nop 1
	global_load_dwordx2 v[84:85], v66, s[16:17] nt
	s_nop 0
	global_load_dwordx2 v[88:89], v66, s[30:31] nt
	global_load_dwordx4 v[6:9], v74, s[14:15] offset:1024 nt
	global_load_dwordx2 v[92:93], v66, s[16:17] offset:512 nt
	global_load_dwordx2 v[90:91], v66, s[30:31] offset:512 nt
	global_load_dwordx4 v[10:13], v74, s[14:15] offset:2048 nt
	global_load_dwordx2 v[94:95], v66, s[16:17] offset:1024 nt
	global_load_dwordx2 v[96:97], v66, s[30:31] offset:1024 nt
	global_load_dwordx4 v[14:17], v74, s[14:15] offset:3072 nt
	global_load_dwordx2 v[100:101], v66, s[16:17] offset:1536 nt
	global_load_dwordx2 v[98:99], v66, s[30:31] offset:1536 nt
	global_load_dwordx4 v[18:21], v68, s[14:15] nt
	global_load_dwordx2 v[102:103], v66, s[16:17] offset:2048 nt
	global_load_dwordx2 v[104:105], v66, s[30:31] offset:2048 nt
	global_load_dwordx4 v[22:25], v126, s[14:15] nt
	global_load_dwordx2 v[108:109], v66, s[16:17] offset:2560 nt
	global_load_dwordx2 v[106:107], v66, s[30:31] offset:2560 nt
	global_load_dwordx4 v[26:29], v128, s[14:15] nt
	global_load_dwordx2 v[110:111], v66, s[16:17] offset:3072 nt
	global_load_dwordx2 v[112:113], v66, s[30:31] offset:3072 nt
	global_load_dwordx4 v[30:33], v130, s[14:15] nt
	global_load_dwordx2 v[116:117], v66, s[16:17] offset:3584 nt
	global_load_dwordx2 v[114:115], v66, s[30:31] offset:3584 nt
	s_lshl_b32 s14, s12, 1
	s_ashr_i32 s15, s14, 31
	s_lshl_b64 s[14:15], s[14:15], 2
	s_add_u32 s14, s25, s14
	s_addc_u32 s15, s26, s15
	v_mov_b32_e32 v36, v226
	v_mov_b32_e32 v37, v227
	ds_read_b32 v1, v1
	s_ashr_i32 s13, s12, 31
	s_lshl_b64 s[12:13], s[12:13], 13
	s_add_u32 s16, s21, s12
	s_addc_u32 s17, s22, s13
	s_lshl_b32 s30, s18, 4
	s_lshl_b32 s34, s18, 5
	s_waitcnt lgkmcnt(0)
	v_add_u32_e32 v38, v36, v1
	v_lshlrev_b32_e32 v1, 2, v35
	v_add_u32_e32 v1, s29, v1
	ds_read_b32 v1, v1
	v_ashrrev_i32_e32 v39, 31, v38
	v_lshlrev_b64 v[38:39], 12, v[38:39]
	v_lshl_add_u64 v[38:39], s[0:1], 0, v[38:39]
	s_waitcnt lgkmcnt(0)
	v_add_u32_e32 v34, v37, v1
	v_ashrrev_i32_e32 v35, 31, v34
	v_lshlrev_b64 v[34:35], 12, v[34:35]
	v_lshl_add_u64 v[40:41], s[0:1], 0, v[34:35]
	v_readfirstlane_b32 s14, v38
	v_readfirstlane_b32 s15, v39
	v_readfirstlane_b32 s12, v40
	v_readfirstlane_b32 s13, v41
	global_load_dwordx4 v[34:37], v74, s[16:17] nt
	v_and_b32_e32 v1, 64, v215
	v_add_u32_e32 v81, 64, v1
	global_load_dwordx2 v[118:119], v66, s[14:15] nt
	s_nop 0
	global_load_dwordx2 v[120:121], v66, s[12:13] nt
	global_load_dwordx4 v[38:41], v74, s[16:17] offset:1024 nt
	global_load_dwordx2 v[138:139], v66, s[14:15] offset:512 nt
	global_load_dwordx2 v[136:137], v66, s[12:13] offset:512 nt
	global_load_dwordx4 v[42:45], v74, s[16:17] offset:2048 nt
	global_load_dwordx2 v[140:141], v66, s[14:15] offset:1024 nt
	global_load_dwordx2 v[142:143], v66, s[12:13] offset:1024 nt
	global_load_dwordx4 v[46:49], v74, s[16:17] offset:3072 nt
	global_load_dwordx2 v[146:147], v66, s[14:15] offset:1536 nt
	global_load_dwordx2 v[144:145], v66, s[12:13] offset:1536 nt
	global_load_dwordx4 v[50:53], v68, s[16:17] nt
	global_load_dwordx2 v[148:149], v66, s[14:15] offset:2048 nt
	global_load_dwordx2 v[150:151], v66, s[12:13] offset:2048 nt
	global_load_dwordx4 v[54:57], v126, s[16:17] nt
	global_load_dwordx2 v[154:155], v66, s[14:15] offset:2560 nt
	global_load_dwordx2 v[152:153], v66, s[12:13] offset:2560 nt
	global_load_dwordx4 v[58:61], v128, s[16:17] nt
	global_load_dwordx2 v[156:157], v66, s[14:15] offset:3072 nt
	global_load_dwordx2 v[158:159], v66, s[12:13] offset:3072 nt
	global_load_dwordx4 v[62:65], v130, s[16:17] nt
	global_load_dwordx2 v[162:163], v66, s[14:15] offset:3584 nt
	global_load_dwordx2 v[160:161], v66, s[12:13] offset:3584 nt
	v_xor_b32_e32 v1, 32, v215
	v_cmp_lt_i32_e32 vcc, v1, v81
	s_add_i32 s12, 0, 0x18000
	s_add_i32 s13, 0, 0x1a000
	v_cndmask_b32_e32 v1, v215, v1, vcc
	v_cmp_lt_i32_e32 vcc, v71, v81
	s_add_i32 s0, s20, s18
	v_add_u32_e32 v207, s12, v86
	v_cndmask_b32_e32 v71, v215, v71, vcc
	v_cmp_lt_i32_e32 vcc, v73, v81
	v_add_u32_e32 v208, s13, v86
	v_or_b32_e32 v86, 0x800, v74
	v_cndmask_b32_e32 v73, v215, v73, vcc
	v_cmp_lt_i32_e32 vcc, v77, v81
	s_lshl_b32 s31, s0, 4
	s_lshl_b32 s0, s0, 5
	v_cndmask_b32_e32 v77, v215, v77, vcc
	v_cmp_lt_i32_e32 vcc, v79, v81
	s_lshl_b32 s1, s19, 2
	v_add_u32_e32 v209, s12, v86
	v_cndmask_b32_e32 v79, v215, v79, vcc
	v_cmp_lt_i32_e32 vcc, v83, v81
	v_add_u32_e32 v210, s13, v86
	v_or_b32_e32 v86, 0xc00, v74
	v_cndmask_b32_e32 v81, v215, v83, vcc
	v_add_u32_e32 v213, s12, v68
	v_add_u32_e32 v231, s13, v68
	v_add_u32_e32 v232, s12, v126
	v_add_u32_e32 v233, s13, v126
	v_add_u32_e32 v234, s12, v128
	v_add_u32_e32 v235, s13, v128
	v_add_u32_e32 v236, s12, v130
	v_add_u32_e32 v237, s13, v130
	v_lshl_add_u64 v[126:127], s[10:11], 0, v[126:127]
	v_lshl_add_u64 v[128:129], s[10:11], 0, v[128:129]
	v_lshl_add_u64 v[130:131], s[10:11], 0, v[130:131]
	v_lshl_add_u64 v[68:69], s[4:5], 0, v[66:67]
	s_mov_b64 s[10:11], 0x12030000
	s_add_i32 s0, s0, s1
	v_lshlrev_b32_e32 v1, 2, v1
	v_lshlrev_b32_e32 v71, 2, v71
	v_lshlrev_b32_e32 v73, 2, v73
	v_lshlrev_b32_e32 v77, 2, v77
	v_lshlrev_b32_e32 v79, 2, v79
	v_lshlrev_b32_e32 v81, 2, v81
	v_add_u32_e32 v83, s12, v74
	v_add_u32_e32 v206, s13, v74
	v_add_u32_e32 v211, s12, v86
	v_add_u32_e32 v212, s13, v86
	v_lshl_add_u64 v[132:133], v[68:69], 0, s[10:11]
	s_or_b32 s10, s0, 3
	s_branch .LBB0_3541

.LBB0_3541:
	s_waitcnt vmcnt(24)
	v_lshlrev_b32_e32 v66, 16, v84
	v_and_b32_e32 v67, 0xffff0000, v84
	v_lshlrev_b32_e32 v68, 16, v88
	v_and_b32_e32 v69, 0xffff0000, v88
	v_pk_add_f32 v[66:67], v[68:69], v[66:67]
	v_lshlrev_b32_e32 v68, 16, v85
	v_and_b32_e32 v69, 0xffff0000, v85
	v_lshlrev_b32_e32 v164, 16, v89
	v_and_b32_e32 v165, 0xffff0000, v89
	v_pk_add_f32 v[68:69], v[164:165], v[68:69]
	v_lshlrev_b32_e32 v164, 16, v92
	v_and_b32_e32 v165, 0xffff0000, v92
	v_lshlrev_b32_e32 v166, 16, v90
	v_and_b32_e32 v167, 0xffff0000, v90
	s_mov_b32 s0, 0x3fd744fd
	v_pk_add_f32 v[164:165], v[166:167], v[164:165]
	v_lshlrev_b32_e32 v166, 16, v91
	v_pk_fma_f32 v[182:183], v[6:7], s[0:1], v[164:165] op_sel_hi:[1,0,1]
	v_lshlrev_b32_e32 v164, 16, v93
	v_and_b32_e32 v165, 0xffff0000, v93
	v_and_b32_e32 v167, 0xffff0000, v91
	v_pk_fma_f32 v[66:67], v[2:3], s[0:1], v[66:67] op_sel_hi:[1,0,1]
	v_pk_add_f32 v[164:165], v[166:167], v[164:165]
	v_pk_fma_f32 v[68:69], v[4:5], s[0:1], v[68:69] op_sel_hi:[1,0,1]
	v_pk_fma_f32 v[188:189], v[8:9], s[0:1], v[164:165] op_sel_hi:[1,0,1]
	v_mov_b32_e32 v164, v182
	v_mov_b32_e32 v165, v66
	v_mov_b32_e32 v166, v183
	v_mov_b32_e32 v167, v67
	v_pk_add_f32 v[164:165], v[164:165], v[166:167]
	v_mov_b32_e32 v166, v188
	v_mov_b32_e32 v167, v68
	v_mov_b32_e32 v168, v189
	v_mov_b32_e32 v169, v69
	v_pk_add_f32 v[166:167], v[166:167], v[168:169]
	v_lshlrev_b32_e32 v168, 16, v96
	v_pk_add_f32 v[164:165], v[164:165], v[166:167]
	v_lshlrev_b32_e32 v166, 16, v94
	v_and_b32_e32 v167, 0xffff0000, v94
	v_and_b32_e32 v169, 0xffff0000, v96
	v_pk_add_f32 v[166:167], v[168:169], v[166:167]
	v_lshlrev_b32_e32 v168, 16, v97
	v_pk_fma_f32 v[184:185], v[10:11], s[0:1], v[166:167] op_sel_hi:[1,0,1]
	v_lshlrev_b32_e32 v166, 16, v95
	v_and_b32_e32 v167, 0xffff0000, v95
	v_and_b32_e32 v169, 0xffff0000, v97
	v_pk_add_f32 v[166:167], v[168:169], v[166:167]
	v_mov_b32_e32 v168, v185
	v_pk_fma_f32 v[190:191], v[12:13], s[0:1], v[166:167] op_sel_hi:[1,0,1]
	v_mov_b32_e32 v166, v184
	v_mov_b32_e32 v167, v190
	v_mov_b32_e32 v169, v191
	v_pk_add_f32 v[166:167], v[166:167], v[168:169]
	v_lshlrev_b32_e32 v168, 16, v100
	v_and_b32_e32 v169, 0xffff0000, v100
	v_lshlrev_b32_e32 v170, 16, v98
	v_and_b32_e32 v171, 0xffff0000, v98
	v_pk_add_f32 v[168:169], v[170:171], v[168:169]
	v_lshlrev_b32_e32 v172, 16, v102
	v_and_b32_e32 v173, 0xffff0000, v102
	v_lshlrev_b32_e32 v174, 16, v104
	v_and_b32_e32 v175, 0xffff0000, v104
	v_pk_fma_f32 v[180:181], v[14:15], s[0:1], v[168:169] op_sel_hi:[1,0,1]
	v_lshlrev_b32_e32 v168, 16, v101
	v_and_b32_e32 v169, 0xffff0000, v101
	v_lshlrev_b32_e32 v170, 16, v99
	v_and_b32_e32 v171, 0xffff0000, v99
	v_pk_add_f32 v[172:173], v[174:175], v[172:173]
	v_pk_add_f32 v[168:169], v[170:171], v[168:169]
	v_pk_fma_f32 v[174:175], v[18:19], s[0:1], v[172:173] op_sel_hi:[1,0,1]
	v_lshlrev_b32_e32 v172, 16, v103
	v_and_b32_e32 v173, 0xffff0000, v103
	v_lshlrev_b32_e32 v176, 16, v105
	v_and_b32_e32 v177, 0xffff0000, v105
	v_pk_fma_f32 v[186:187], v[16:17], s[0:1], v[168:169] op_sel_hi:[1,0,1]
	v_pk_add_f32 v[172:173], v[176:177], v[172:173]
	v_add_f32_e32 v75, 0, v165
	v_pk_add_f32 v[166:167], v[166:167], v[166:167] op_sel_hi:[0,1]
	v_pk_add_f32 v[168:169], v[180:181], v[180:181] op_sel_hi:[0,1]
	v_pk_add_f32 v[170:171], v[186:187], v[186:187] op_sel_hi:[0,1]
	v_pk_fma_f32 v[178:179], v[20:21], s[0:1], v[172:173] op_sel_hi:[1,0,1]
	v_add_f32_e32 v165, v164, v75
	v_mov_b32_e32 v168, v174
	v_mov_b32_e32 v170, v175
	v_mov_b32_e32 v166, v178
	v_mov_b32_e32 v164, v179
	v_pk_add_f32 v[168:169], v[168:169], v[170:171]
	v_pk_add_f32 v[164:165], v[166:167], v[164:165]
	v_lshlrev_b32_e32 v166, 16, v106
	v_pk_add_f32 v[164:165], v[168:169], v[164:165]
	v_and_b32_e32 v167, 0xffff0000, v106
	v_pk_add_f32 v[192:193], v[164:165], v[164:165] op_sel_hi:[0,1]
	v_lshlrev_b32_e32 v164, 16, v108
	v_and_b32_e32 v165, 0xffff0000, v108
	v_pk_add_f32 v[164:165], v[166:167], v[164:165]
	v_lshlrev_b32_e32 v166, 16, v107
	v_pk_fma_f32 v[170:171], v[22:23], s[0:1], v[164:165] op_sel_hi:[1,0,1]
	v_lshlrev_b32_e32 v164, 16, v109
	v_and_b32_e32 v165, 0xffff0000, v109
	v_and_b32_e32 v167, 0xffff0000, v107
	v_pk_add_f32 v[164:165], v[166:167], v[164:165]
	v_mov_b32_e32 v166, v171
	v_pk_fma_f32 v[176:177], v[24:25], s[0:1], v[164:165] op_sel_hi:[1,0,1]
	v_mov_b32_e32 v164, v170
	v_mov_b32_e32 v165, v176
	v_mov_b32_e32 v167, v177
	v_pk_add_f32 v[164:165], v[164:165], v[166:167]
	v_lshlrev_b32_e32 v166, 16, v112
	v_pk_add_f32 v[194:195], v[164:165], v[164:165] op_sel_hi:[0,1]
	v_lshlrev_b32_e32 v164, 16, v110
	v_and_b32_e32 v165, 0xffff0000, v110
	v_and_b32_e32 v167, 0xffff0000, v112
	v_pk_add_f32 v[164:165], v[166:167], v[164:165]
	v_lshlrev_b32_e32 v166, 16, v113
	v_pk_fma_f32 v[168:169], v[26:27], s[0:1], v[164:165] op_sel_hi:[1,0,1]
	v_lshlrev_b32_e32 v164, 16, v111
	v_and_b32_e32 v165, 0xffff0000, v111
	v_and_b32_e32 v167, 0xffff0000, v113
	v_pk_add_f32 v[164:165], v[166:167], v[164:165]
	v_lshlrev_b32_e32 v166, 16, v114
	v_pk_fma_f32 v[172:173], v[28:29], s[0:1], v[164:165] op_sel_hi:[1,0,1]
	v_lshlrev_b32_e32 v164, 16, v116
	v_and_b32_e32 v165, 0xffff0000, v116
	v_and_b32_e32 v167, 0xffff0000, v114
	v_pk_add_f32 v[164:165], v[166:167], v[164:165]
	v_lshlrev_b32_e32 v166, 16, v117
	v_and_b32_e32 v167, 0xffff0000, v117
	v_lshlrev_b32_e32 v200, 16, v115
	v_and_b32_e32 v201, 0xffff0000, v115
	v_pk_add_f32 v[166:167], v[200:201], v[166:167]
	v_pk_add_f32 v[196:197], v[168:169], v[168:169] op_sel_hi:[0,1]
	v_pk_add_f32 v[198:199], v[172:173], v[172:173] op_sel_hi:[0,1]
	v_pk_fma_f32 v[164:165], v[30:31], s[0:1], v[164:165] op_sel_hi:[1,0,1]
	v_pk_fma_f32 v[166:167], v[32:33], s[0:1], v[166:167] op_sel_hi:[1,0,1]
	v_mov_b32_e32 v196, v164
	v_mov_b32_e32 v198, v165
	v_mov_b32_e32 v194, v166
	v_mov_b32_e32 v192, v167
	v_pk_add_f32 v[196:197], v[196:197], v[198:199]
	v_pk_add_f32 v[192:193], v[194:195], v[192:193]
	s_mov_b32 s0, 0x800000
	v_pk_add_f32 v[192:193], v[196:197], v[192:193]
	s_add_i32 s12, s27, s28
	v_add_f32_e32 v75, v192, v193
	ds_bpermute_b32 v86, v1, v75
	s_ashr_i32 s13, s12, 31
	s_lshl_b64 s[14:15], s[12:13], 11
	s_waitcnt lgkmcnt(0)
	v_add_f32_e32 v75, v75, v86
	ds_bpermute_b32 v86, v71, v75
	s_waitcnt lgkmcnt(0)
	v_add_f32_e32 v75, v75, v86
	ds_bpermute_b32 v86, v73, v75
	s_waitcnt lgkmcnt(0)
	v_add_f32_e32 v75, v75, v86
	ds_bpermute_b32 v86, v77, v75
	s_waitcnt lgkmcnt(0)
	v_add_f32_e32 v75, v75, v86
	ds_bpermute_b32 v86, v79, v75
	s_waitcnt lgkmcnt(0)
	v_add_f32_e32 v75, v75, v86
	ds_bpermute_b32 v86, v81, v75
	s_waitcnt lgkmcnt(0)
	v_add_f32_e32 v75, v75, v86
	v_fmamk_f32 v67, v75, 0xba000000, v67
	v_fmamk_f32 v69, v75, 0xba000000, v69
	v_fmac_f32_e32 v66, 0xba000000, v75
	v_fmamk_f32 v193, v75, 0xba000000, v183
	v_fmac_f32_e32 v182, 0xba000000, v75
	v_mov_b32_e32 v192, v67
	v_fmac_f32_e32 v68, 0xba000000, v75
	v_fmamk_f32 v201, v75, 0xba000000, v189
	v_fmac_f32_e32 v188, 0xba000000, v75
	v_mov_b32_e32 v194, v66
	v_mov_b32_e32 v195, v182
	v_pk_mul_f32 v[196:197], v[192:193], v[192:193]
	v_mov_b32_e32 v200, v69
	v_pk_fma_f32 v[194:195], v[194:195], v[194:195], v[196:197]
	v_mov_b32_e32 v196, v68
	v_mov_b32_e32 v197, v188
	v_pk_mul_f32 v[198:199], v[200:201], v[200:201]
	v_fmamk_f32 v191, v75, 0xba000000, v191
	v_pk_fma_f32 v[196:197], v[196:197], v[196:197], v[198:199]
	v_fmac_f32_e32 v190, 0xba000000, v75
	v_fmamk_f32 v185, v75, 0xba000000, v185
	v_fmac_f32_e32 v184, 0xba000000, v75
	v_pk_add_f32 v[194:195], v[194:195], v[196:197]
	v_pk_mul_f32 v[196:197], v[190:191], v[190:191]
	v_pk_mul_f32 v[198:199], v[184:185], v[184:185]
	v_fmac_f32_e32 v180, 0xba000000, v75
	v_pk_mov_b32 v[202:203], v[198:199], v[196:197] op_sel:[1,0]
	v_mov_b32_e32 v199, v197
	v_fmac_f32_e32 v186, 0xba000000, v75
	v_fmamk_f32 v181, v75, 0xba000000, v181
	v_mul_f32_e32 v86, v180, v180
	v_pk_add_f32 v[196:197], v[202:203], v[198:199]
	v_fmamk_f32 v187, v75, 0xba000000, v187
	v_pk_fma_f32 v[198:199], v[180:181], v[180:181], v[86:87] op_sel_hi:[1,1,0]
	v_mul_f32_e32 v86, v186, v186
	v_pk_add_f32 v[194:195], v[194:195], v[194:195] op_sel_hi:[0,1]
	v_pk_add_f32 v[196:197], v[196:197], v[196:197] op_sel_hi:[0,1]
	v_pk_fma_f32 v[202:203], v[186:187], v[186:187], v[86:87] op_sel_hi:[1,1,0]
	v_fmamk_f32 v179, v75, 0xba000000, v179
	v_fmac_f32_e32 v178, 0xba000000, v75
	v_fmamk_f32 v175, v75, 0xba000000, v175
	v_fmac_f32_e32 v174, 0xba000000, v75
	v_mul_f32_e32 v198, v174, v174
	v_mul_f32_e32 v202, v175, v175
	v_mul_f32_e32 v196, v178, v178
	v_mul_f32_e32 v194, v179, v179
	v_pk_add_f32 v[198:199], v[198:199], v[202:203]
	v_pk_add_f32 v[194:195], v[196:197], v[194:195]
	v_fmamk_f32 v177, v75, 0xba000000, v177
	v_fmac_f32_e32 v176, 0xba000000, v75
	v_fmamk_f32 v171, v75, 0xba000000, v171
	v_fmac_f32_e32 v170, 0xba000000, v75
	v_pk_add_f32 v[194:195], v[198:199], v[194:195]
	v_pk_mul_f32 v[196:197], v[176:177], v[176:177]
	v_pk_mul_f32 v[198:199], v[170:171], v[170:171]
	v_fmac_f32_e32 v168, 0xba000000, v75
	v_pk_mov_b32 v[202:203], v[198:199], v[196:197] op_sel:[1,0]
	v_mov_b32_e32 v199, v197
	v_fmac_f32_e32 v172, 0xba000000, v75
	v_fmamk_f32 v169, v75, 0xba000000, v169
	v_mul_f32_e32 v86, v168, v168
	v_pk_add_f32 v[196:197], v[202:203], v[198:199]
	v_fmamk_f32 v173, v75, 0xba000000, v173
	v_pk_fma_f32 v[198:199], v[168:169], v[168:169], v[86:87] op_sel_hi:[1,1,0]
	v_mul_f32_e32 v86, v172, v172
	v_pk_add_f32 v[194:195], v[194:195], v[194:195] op_sel_hi:[0,1]
	v_pk_add_f32 v[196:197], v[196:197], v[196:197] op_sel_hi:[0,1]
	v_pk_fma_f32 v[202:203], v[172:173], v[172:173], v[86:87] op_sel_hi:[1,1,0]
	v_fmamk_f32 v167, v75, 0xba000000, v167
	v_fmac_f32_e32 v166, 0xba000000, v75
	v_fmamk_f32 v165, v75, 0xba000000, v165
	v_fmac_f32_e32 v164, 0xba000000, v75
	v_mul_f32_e32 v198, v164, v164
	v_mul_f32_e32 v202, v165, v165
	v_mul_f32_e32 v196, v166, v166
	v_mul_f32_e32 v194, v167, v167
	v_pk_add_f32 v[198:199], v[198:199], v[202:203]
	v_pk_add_f32 v[194:195], v[196:197], v[194:195]
	s_nop 0
	v_pk_add_f32 v[194:195], v[198:199], v[194:195]
	s_nop 0
	v_add_f32_e32 v75, v194, v195
	ds_bpermute_b32 v86, v1, v75
	ds_read_b128 v[194:197], v83
	ds_read_b128 v[202:205], v206
	s_waitcnt lgkmcnt(2)
	v_add_f32_e32 v75, v75, v86
	ds_bpermute_b32 v86, v71, v75
	s_waitcnt lgkmcnt(0)
	v_add_f32_e32 v75, v75, v86
	ds_bpermute_b32 v86, v73, v75
	s_waitcnt lgkmcnt(0)
	v_add_f32_e32 v75, v75, v86
	ds_bpermute_b32 v86, v77, v75
	s_waitcnt lgkmcnt(0)
	v_add_f32_e32 v75, v75, v86
	ds_bpermute_b32 v86, v79, v75
	s_waitcnt lgkmcnt(0)
	v_add_f32_e32 v75, v75, v86
	ds_bpermute_b32 v86, v81, v75
	s_waitcnt lgkmcnt(0)
	v_add_f32_e32 v75, v75, v86
	v_fmamk_f32 v75, v75, 0x3a000000, v214
	v_mul_f32_e32 v86, 0x4b800000, v75
	v_cmp_gt_f32_e32 vcc, s0, v75
	s_lshl_b64 s[0:1], s[12:13], 13
	s_add_u32 s16, s6, s0
	v_cndmask_b32_e32 v75, v75, v86, vcc
	v_rsq_f32_e32 v75, v75
	s_addc_u32 s17, s7, s1
	v_mul_f32_e32 v86, 0x45800000, v75
	v_cndmask_b32_e32 v192, v75, v86, vcc
	v_pk_mul_f32 v[66:67], v[66:67], v[192:193] op_sel_hi:[1,0]
	v_pk_mul_f32 v[68:69], v[68:69], v[192:193] op_sel_hi:[1,0]
	v_cndmask_b32_e64 v75, 0, 1, s[8:9]
	v_pk_fma_f32 v[68:69], v[196:197], v[68:69], v[204:205]
	v_pk_fma_f32 v[66:67], v[194:195], v[66:67], v[202:203]
	v_lshlrev_b32_e32 v86, 2, v72
	v_cmp_ne_u32_e64 s[0:1], 1, v75
	s_andn2_b64 vcc, exec, s[8:9]
	global_store_dwordx4 v86, v[66:69], s[16:17]
	s_cbranch_vccnz .LBB0_3543
	v_lshl_add_u64 v[194:195], s[14:15], 2, v[122:123]
	global_store_dwordx4 v[194:195], v[66:69], off

.LBB0_3573:
	s_add_i32 s20, s20, s18
	s_cmpk_gt_i32 s20, 0x1ff
	s_cselect_b64 s[0:1], -1, 0
	s_and_b64 vcc, exec, s[0:1]
	v_cvt_pk_bf16_f32 v66, v66, v67
	v_cvt_pk_bf16_f32 v67, v68, v69
	global_store_dwordx2 v[194:195], v[66:67], off offset:3584
	s_cbranch_vccnz .LBB0_3540
	s_cmp_eq_u32 s32, 1
	s_cbranch_scc1 .Lln2_pf_fast
	s_add_i32 s14, s10, -3
	s_ashr_i32 s15, s14, 31
	s_add_i32 s12, s31, s28
	s_lshl_b64 s[14:15], s[14:15], 2
	s_add_u32 s16, s23, s14
	s_addc_u32 s17, s24, s15
	global_load_dword v2, v87, s[16:17]
	s_add_i32 s16, s10, -2
	s_ashr_i32 s17, s16, 31
	s_lshl_b64 s[16:17], s[16:17], 2
	s_add_u32 s36, s23, s16
	s_addc_u32 s37, s24, s17
	s_add_u32 s14, s25, s14
	s_addc_u32 s15, s26, s15
	global_load_dword v4, v87, s[36:37]
	global_load_dword v3, v87, s[14:15]
	s_add_u32 s14, s25, s16
	s_addc_u32 s15, s26, s17
	s_ashr_i32 s13, s12, 31
	s_waitcnt vmcnt(2)
	v_lshlrev_b32_e32 v2, 2, v2
	v_add_u32_e32 v2, s29, v2
	ds_read_b32 v2, v2
	s_waitcnt vmcnt(0) lgkmcnt(0)
	v_add_u32_e32 v2, v3, v2
	v_ashrrev_i32_e32 v3, 31, v2
	v_lshlrev_b64 v[6:7], 12, v[2:3]
	global_load_dword v3, v87, s[14:15]
	v_lshlrev_b32_e32 v2, 2, v4
	v_add_u32_e32 v2, s29, v2
	ds_read_b32 v2, v2
	s_lshl_b64 s[14:15], s[12:13], 13
	s_add_u32 s14, s21, s14
	s_addc_u32 s15, s22, s15
	v_lshl_add_u64 v[34:35], v[134:135], 0, v[6:7]
	s_add_i32 s12, s12, 1
	global_load_dwordx2 v[84:85], v[34:35], off nt
	s_waitcnt vmcnt(1) lgkmcnt(0)
	v_add_u32_e32 v2, v3, v2
	v_ashrrev_i32_e32 v3, 31, v2
	v_lshlrev_b64 v[8:9], 12, v[2:3]
	v_lshl_add_u64 v[30:31], v[134:135], 0, v[8:9]
	global_load_dwordx4 v[2:5], v86, s[14:15] nt
	global_load_dwordx2 v[88:89], v[30:31], off nt
	global_load_dwordx2 v[90:91], v[30:31], off offset:512 nt
	global_load_dwordx4 v[6:9], v86, s[14:15] offset:1024 nt
	global_load_dwordx2 v[92:93], v[34:35], off offset:512 nt
	global_load_dwordx4 v[10:13], v86, s[14:15] offset:2048 nt
	global_load_dwordx2 v[94:95], v[34:35], off offset:1024 nt
	global_load_dwordx2 v[96:97], v[30:31], off offset:1024 nt
	global_load_dwordx2 v[98:99], v[30:31], off offset:1536 nt
	global_load_dwordx4 v[14:17], v86, s[14:15] offset:3072 nt
	global_load_dwordx2 v[100:101], v[34:35], off offset:1536 nt
	global_load_dwordx4 v[18:21], v239, s[14:15] nt
	global_load_dwordx2 v[102:103], v[34:35], off offset:2048 nt
	global_load_dwordx2 v[104:105], v[30:31], off offset:2048 nt
	global_load_dwordx2 v[106:107], v[30:31], off offset:2560 nt
	global_load_dwordx4 v[22:25], v240, s[14:15] nt
	global_load_dwordx2 v[108:109], v[34:35], off offset:2560 nt
	global_load_dwordx4 v[26:29], v238, s[14:15] nt
	global_load_dwordx2 v[110:111], v[34:35], off offset:3072 nt
	global_load_dwordx2 v[112:113], v[30:31], off offset:3072 nt
	global_load_dwordx2 v[114:115], v[30:31], off offset:3584 nt
	s_nop 0
	global_load_dwordx4 v[30:33], v75, s[14:15] nt
	global_load_dwordx2 v[116:117], v[34:35], off offset:3584 nt
	s_add_i32 s14, s10, -1
	s_ashr_i32 s15, s14, 31
	s_lshl_b64 s[14:15], s[14:15], 2
	s_add_u32 s16, s23, s14
	s_addc_u32 s17, s24, s15
	global_load_dword v34, v87, s[16:17]
	s_ashr_i32 s11, s10, 31
	s_lshl_b64 s[16:17], s[10:11], 2
	s_add_u32 s36, s23, s16
	s_addc_u32 s37, s24, s17
	s_add_u32 s14, s25, s14
	s_addc_u32 s15, s26, s15
	global_load_dword v36, v87, s[36:37]
	global_load_dword v35, v87, s[14:15]
	s_add_u32 s14, s25, s16
	s_addc_u32 s15, s26, s17
	s_ashr_i32 s13, s12, 31
	s_lshl_b64 s[12:13], s[12:13], 13
	s_add_u32 s12, s21, s12
	s_addc_u32 s13, s22, s13
	s_waitcnt vmcnt(2)
	v_lshlrev_b32_e32 v34, 2, v34
	v_add_u32_e32 v34, s29, v34
	ds_read_b32 v34, v34
	s_waitcnt vmcnt(0) lgkmcnt(0)
	v_add_u32_e32 v34, v35, v34
	v_ashrrev_i32_e32 v35, 31, v34
	v_lshlrev_b64 v[38:39], 12, v[34:35]
	global_load_dword v35, v87, s[14:15]
	v_lshlrev_b32_e32 v34, 2, v36
	v_add_u32_e32 v34, s29, v34
	ds_read_b32 v34, v34
	v_lshl_add_u64 v[66:67], v[134:135], 0, v[38:39]
	global_load_dwordx2 v[118:119], v[66:67], off nt
	s_waitcnt vmcnt(1) lgkmcnt(0)
	v_add_u32_e32 v34, v35, v34
	v_ashrrev_i32_e32 v35, 31, v34
	v_lshlrev_b64 v[40:41], 12, v[34:35]
	v_lshl_add_u64 v[62:63], v[134:135], 0, v[40:41]
	global_load_dwordx4 v[34:37], v86, s[12:13] nt
	global_load_dwordx2 v[120:121], v[62:63], off nt
	global_load_dwordx2 v[136:137], v[62:63], off offset:512 nt
	global_load_dwordx4 v[38:41], v86, s[12:13] offset:1024 nt
	global_load_dwordx2 v[138:139], v[66:67], off offset:512 nt
	global_load_dwordx4 v[42:45], v86, s[12:13] offset:2048 nt
	global_load_dwordx2 v[140:141], v[66:67], off offset:1024 nt
	global_load_dwordx2 v[142:143], v[62:63], off offset:1024 nt
	global_load_dwordx2 v[144:145], v[62:63], off offset:1536 nt
	global_load_dwordx4 v[46:49], v86, s[12:13] offset:3072 nt
	global_load_dwordx2 v[146:147], v[66:67], off offset:1536 nt
	global_load_dwordx4 v[50:53], v239, s[12:13] nt
	global_load_dwordx2 v[148:149], v[66:67], off offset:2048 nt
	global_load_dwordx2 v[150:151], v[62:63], off offset:2048 nt
	global_load_dwordx2 v[152:153], v[62:63], off offset:2560 nt
	global_load_dwordx4 v[54:57], v240, s[12:13] nt
	global_load_dwordx2 v[154:155], v[66:67], off offset:2560 nt
	global_load_dwordx4 v[58:61], v238, s[12:13] nt
	global_load_dwordx2 v[156:157], v[66:67], off offset:3072 nt
	global_load_dwordx2 v[158:159], v[62:63], off offset:3072 nt
	global_load_dwordx2 v[160:161], v[62:63], off offset:3584 nt
	s_nop 0
	global_load_dwordx4 v[62:65], v75, s[12:13] nt
	global_load_dwordx2 v[162:163], v[66:67], off offset:3584 nt
	s_branch .LBB0_3540
.Lln2_pf_fast:
	s_mov_b32 s32, 0
	s_add_i32 s14, s10, -3
	s_ashr_i32 s15, s14, 31
	s_add_i32 s12, s31, s28
	s_lshl_b64 s[14:15], s[14:15], 2
	s_add_u32 s16, s23, s14
	s_addc_u32 s17, s24, s15
	v_mov_b32_e32 v2, v242
	s_add_i32 s16, s10, -2
	s_ashr_i32 s17, s16, 31
	s_lshl_b64 s[16:17], s[16:17], 2
	s_add_u32 s36, s23, s16
	s_addc_u32 s37, s24, s17
	s_add_u32 s14, s25, s14
	s_addc_u32 s15, s26, s15
	v_mov_b32_e32 v4, v243
	v_mov_b32_e32 v3, v246
	s_add_u32 s14, s25, s16
	s_addc_u32 s15, s26, s17
	s_ashr_i32 s13, s12, 31
	v_lshlrev_b32_e32 v2, 2, v2
	v_add_u32_e32 v2, s29, v2
	ds_read_b32 v2, v2
	s_waitcnt lgkmcnt(0)
	v_add_u32_e32 v2, v3, v2
	v_ashrrev_i32_e32 v3, 31, v2
	v_lshlrev_b64 v[6:7], 12, v[2:3]
	v_mov_b32_e32 v3, v247
	v_lshlrev_b32_e32 v2, 2, v4
	v_add_u32_e32 v2, s29, v2
	ds_read_b32 v2, v2
	s_lshl_b64 s[14:15], s[12:13], 13
	s_add_u32 s14, s21, s14
	s_addc_u32 s15, s22, s15
	v_lshl_add_u64 v[34:35], v[134:135], 0, v[6:7]
	s_add_i32 s12, s12, 1
	s_waitcnt vmcnt(39)
	global_load_dwordx2 v[84:85], v[34:35], off nt
	s_waitcnt lgkmcnt(0)
	v_add_u32_e32 v2, v3, v2
	v_ashrrev_i32_e32 v3, 31, v2
	v_lshlrev_b64 v[8:9], 12, v[2:3]
	v_lshl_add_u64 v[30:31], v[134:135], 0, v[8:9]
	global_load_dwordx4 v[2:5], v86, s[14:15] nt
	global_load_dwordx2 v[88:89], v[30:31], off nt
	global_load_dwordx2 v[90:91], v[30:31], off offset:512 nt
	global_load_dwordx4 v[6:9], v86, s[14:15] offset:1024 nt
	global_load_dwordx2 v[92:93], v[34:35], off offset:512 nt
	global_load_dwordx4 v[10:13], v86, s[14:15] offset:2048 nt
	global_load_dwordx2 v[94:95], v[34:35], off offset:1024 nt
	global_load_dwordx2 v[96:97], v[30:31], off offset:1024 nt
	global_load_dwordx2 v[98:99], v[30:31], off offset:1536 nt
	global_load_dwordx4 v[14:17], v86, s[14:15] offset:3072 nt
	global_load_dwordx2 v[100:101], v[34:35], off offset:1536 nt
	global_load_dwordx4 v[18:21], v239, s[14:15] nt
	global_load_dwordx2 v[102:103], v[34:35], off offset:2048 nt
	global_load_dwordx2 v[104:105], v[30:31], off offset:2048 nt
	global_load_dwordx2 v[106:107], v[30:31], off offset:2560 nt
	global_load_dwordx4 v[22:25], v240, s[14:15] nt
	global_load_dwordx2 v[108:109], v[34:35], off offset:2560 nt
	global_load_dwordx4 v[26:29], v238, s[14:15] nt
	global_load_dwordx2 v[110:111], v[34:35], off offset:3072 nt
	global_load_dwordx2 v[112:113], v[30:31], off offset:3072 nt
	global_load_dwordx2 v[114:115], v[30:31], off offset:3584 nt
	s_nop 0
	global_load_dwordx4 v[30:33], v75, s[14:15] nt
	global_load_dwordx2 v[116:117], v[34:35], off offset:3584 nt
	s_add_i32 s14, s10, -1
	s_ashr_i32 s15, s14, 31
	s_lshl_b64 s[14:15], s[14:15], 2
	s_add_u32 s16, s23, s14
	s_addc_u32 s17, s24, s15
	v_mov_b32_e32 v34, v244
	s_ashr_i32 s11, s10, 31
	s_lshl_b64 s[16:17], s[10:11], 2
	s_add_u32 s36, s23, s16
	s_addc_u32 s37, s24, s17
	s_add_u32 s14, s25, s14
	s_addc_u32 s15, s26, s15
	v_mov_b32_e32 v36, v245
	v_mov_b32_e32 v35, v248
	s_add_u32 s14, s25, s16
	s_addc_u32 s15, s26, s17
	s_ashr_i32 s13, s12, 31
	s_lshl_b64 s[12:13], s[12:13], 13
	s_add_u32 s12, s21, s12
	s_addc_u32 s13, s22, s13
	v_lshlrev_b32_e32 v34, 2, v34
	v_add_u32_e32 v34, s29, v34
	ds_read_b32 v34, v34
	s_waitcnt lgkmcnt(0)
	v_add_u32_e32 v34, v35, v34
	v_ashrrev_i32_e32 v35, 31, v34
	v_lshlrev_b64 v[38:39], 12, v[34:35]
	v_mov_b32_e32 v35, v249
	v_lshlrev_b32_e32 v34, 2, v36
	v_add_u32_e32 v34, s29, v34
	ds_read_b32 v34, v34
	v_lshl_add_u64 v[66:67], v[134:135], 0, v[38:39]
	s_waitcnt vmcnt(39)
	global_load_dwordx2 v[118:119], v[66:67], off nt
	s_waitcnt lgkmcnt(0)
	v_add_u32_e32 v34, v35, v34
	v_ashrrev_i32_e32 v35, 31, v34
	v_lshlrev_b64 v[40:41], 12, v[34:35]
	v_lshl_add_u64 v[62:63], v[134:135], 0, v[40:41]
	global_load_dwordx4 v[34:37], v86, s[12:13] nt
	global_load_dwordx2 v[120:121], v[62:63], off nt
	global_load_dwordx2 v[136:137], v[62:63], off offset:512 nt
	global_load_dwordx4 v[38:41], v86, s[12:13] offset:1024 nt
	global_load_dwordx2 v[138:139], v[66:67], off offset:512 nt
	global_load_dwordx4 v[42:45], v86, s[12:13] offset:2048 nt
	global_load_dwordx2 v[140:141], v[66:67], off offset:1024 nt
	global_load_dwordx2 v[142:143], v[62:63], off offset:1024 nt
	global_load_dwordx2 v[144:145], v[62:63], off offset:1536 nt
	global_load_dwordx4 v[46:49], v86, s[12:13] offset:3072 nt
	global_load_dwordx2 v[146:147], v[66:67], off offset:1536 nt
	global_load_dwordx4 v[50:53], v239, s[12:13] nt
	global_load_dwordx2 v[148:149], v[66:67], off offset:2048 nt
	global_load_dwordx2 v[150:151], v[62:63], off offset:2048 nt
	global_load_dwordx2 v[152:153], v[62:63], off offset:2560 nt
	global_load_dwordx4 v[54:57], v240, s[12:13] nt
	global_load_dwordx2 v[154:155], v[66:67], off offset:2560 nt
	global_load_dwordx4 v[58:61], v238, s[12:13] nt
	global_load_dwordx2 v[156:157], v[66:67], off offset:3072 nt
	global_load_dwordx2 v[158:159], v[62:63], off offset:3072 nt
	global_load_dwordx2 v[160:161], v[62:63], off offset:3584 nt
	s_nop 0
	global_load_dwordx4 v[62:65], v75, s[12:13] nt
	global_load_dwordx2 v[162:163], v[66:67], off offset:3584 nt
	s_branch .LBB0_3540
